# gqa16 tile loop: second half of P.V streams its V fragments through four quads so v168-175 free up early; exps spread one per MFMA over MFMAs 3-32 instead of two per MFMA at the end
# speedup vs baseline: 1.0015x; 1.0015x over previous
; #define SBAR() __builtin_amdgcn_sched_barrier(0)
; template <int LDQ, int LDK, int LDO>
; __device__ __forceinline__ void attn_gqa16_body(const bf16* __restrict__ Qb, const bf16* __restrict__ Kh, const bf16* __restrict__ Vh, bf16* __restrict__ Ob, int seq, char* lds, float mref) {
;     ...
;     HPACK();
;     __syncthreads();
;     const bool more = t + 1 < NT;
;     if (more) HQK((t + 1) & 1);
;     const int vb = vb0 + (t & 1) * (int)G16_V;
;     SBAR(); pv16<0>(o, vb, pb); SBAR();
.LBB0_650:
	s_add_i32 s17, s16, 1
	s_and_b32 s16, s16, 1
	s_and_b32 s46, 1, s17
	s_cmp_eq_u32 s46, 1
	s_cselect_b32 s85, s86, s84
	s_cselect_b32 s46, 0x4400, 0
	v_add_u32_e32 v189, s46, v182
	v_cvt_pk_bf16_f32 v124, v134, v138
	v_cvt_pk_bf16_f32 v125, v136, v140
	v_cvt_pk_bf16_f32 v128, v135, v139
	v_cvt_pk_bf16_f32 v129, v137, v141
	s_waitcnt vmcnt(2)
	s_barrier
	ds_read_b128 v[130:133], v189 offset:33280
	ds_read_b128 v[146:149], v189 offset:33344
	ds_read_b128 v[200:203], v189 offset:37632
	ds_read_b128 v[204:207], v189 offset:37696
	ds_read_b128 v[212:215], v189 offset:41984
	ds_read_b128 v[216:219], v189 offset:42048
	ds_read_b128 v[224:227], v189 offset:46336
	ds_read_b128 v[228:231], v189 offset:46400
	s_mov_b32 m0, s85
	s_nop 0
	global_load_lds_dwordx4 v253, s[74:75]
	s_add_i32 m0, s85, 0x400
	s_nop 0
	global_load_lds_dwordx4 v253, s[76:77]
	s_add_u32 s74, s74, 0x90000
	s_addc_u32 s75, s75, 0
	s_add_u32 s76, s76, 0x90000
	s_addc_u32 s77, s77, 0
	s_waitcnt lgkmcnt(7)
	v_mfma_f32_16x16x32_bf16 v[196:199], v[130:133], v[30:33], v[248:251]
	v_add_f32_e64 v134, v134, v138
	v_add_f32_e64 v135, v135, v139
	v_pk_add_f32 v[136:137], v[136:137], v[140:141]
	s_mul_i32 s46, s16, 0x4100
	v_mfma_f32_16x16x32_bf16 v[130:133], v[130:133], v[38:41], v[248:251]
	v_cvt_pk_bf16_f32 v114, v246, v152
	s_waitcnt lgkmcnt(5)
	v_mfma_f32_16x16x32_bf16 v[208:211], v[200:203], v[30:33], v[248:251]
	v_cvt_pk_bf16_f32 v115, v240, v160
	v_mfma_f32_16x16x32_bf16 v[200:203], v[200:203], v[38:41], v[248:251]
	v_cvt_pk_bf16_f32 v116, v168, v170
	s_waitcnt lgkmcnt(3)
	v_mfma_f32_16x16x32_bf16 v[220:223], v[212:215], v[30:33], v[248:251]
	v_cvt_pk_bf16_f32 v117, v242, v244
	v_mfma_f32_16x16x32_bf16 v[212:215], v[212:215], v[38:41], v[248:251]
	v_cvt_pk_bf16_f32 v118, v247, v153
	s_waitcnt lgkmcnt(1)
	v_mfma_f32_16x16x32_bf16 v[232:235], v[224:227], v[30:33], v[248:251]
	v_cvt_pk_bf16_f32 v119, v241, v161
	v_mfma_f32_16x16x32_bf16 v[224:227], v[224:227], v[38:41], v[248:251]
	v_cvt_pk_bf16_f32 v120, v169, v171
	v_mfma_f32_16x16x32_bf16 v[196:199], v[146:149], v[18:21], v[196:199]
	v_cvt_pk_bf16_f32 v121, v243, v245
	v_mfma_f32_16x16x32_bf16 v[130:133], v[146:149], v[22:25], v[130:133]
	v_cvt_pk_bf16_f32 v122, v142, v172
	v_mfma_f32_16x16x32_bf16 v[146:149], v[204:207], v[18:21], v[208:211]
	v_cvt_pk_bf16_f32 v123, v144, v174
	v_mfma_f32_16x16x32_bf16 v[200:203], v[204:207], v[22:25], v[200:203]
	v_cvt_pk_bf16_f32 v126, v143, v173
	v_mfma_f32_16x16x32_bf16 v[204:207], v[216:219], v[18:21], v[220:223]
	v_cvt_pk_bf16_f32 v127, v145, v175
	v_mfma_f32_16x16x32_bf16 v[208:211], v[216:219], v[22:25], v[212:215]
	s_waitcnt lgkmcnt(0)
	v_mfma_f32_16x16x32_bf16 v[216:219], v[228:231], v[22:25], v[224:227]
	ds_read_b128 v[220:223], v189 offset:33408
	s_nop 1
	ds_read_b128 v[224:227], v189 offset:33472
	v_mfma_f32_16x16x32_bf16 v[212:215], v[228:231], v[18:21], v[232:235]
	s_waitcnt lgkmcnt(1)
	v_mfma_f32_16x16x32_bf16 v[196:199], v[220:223], v[10:13], v[196:199]
	v_mfma_f32_16x16x32_bf16 v[130:133], v[220:223], v[14:17], v[130:133]
	ds_read_b128 v[220:223], v189 offset:37760
	ds_read_b128 v[228:231], v189 offset:37824
	s_waitcnt lgkmcnt(1)
	v_mfma_f32_16x16x32_bf16 v[146:149], v[220:223], v[10:13], v[146:149]
	v_mfma_f32_16x16x32_bf16 v[200:203], v[220:223], v[14:17], v[200:203]
	ds_read_b128 v[220:223], v189 offset:42112
	ds_read_b128 v[232:235], v189 offset:42176
	s_waitcnt lgkmcnt(1)
	v_mfma_f32_16x16x32_bf16 v[204:207], v[220:223], v[10:13], v[204:207]
	v_mfma_f32_16x16x32_bf16 v[208:211], v[220:223], v[14:17], v[208:211]
	ds_read_b128 v[220:223], v189 offset:46464
	ds_read_b128 v[236:239], v189 offset:46528
	v_add_u32_e32 v189, s46, v183
	s_waitcnt lgkmcnt(1)
	v_mfma_f32_16x16x32_bf16 v[212:215], v[220:223], v[10:13], v[212:215]
	v_mfma_f32_16x16x32_bf16 v[216:219], v[220:223], v[14:17], v[216:219]
	v_mfma_f32_16x16x32_bf16 v[220:223], v[224:227], v[6:9], v[130:133]
	s_nop 2
	v_add_f32_e64 v130, v246, v152
	v_add_f32_e64 v131, v247, v153
	v_pk_add_f32 v[132:133], v[240:241], v[160:161]
	v_pk_add_f32 v[152:153], v[168:169], v[170:171]
	v_pk_add_f32 v[156:157], v[242:243], v[244:245]
	v_pk_add_f32 v[158:159], v[142:143], v[172:173]
	v_pk_add_f32 v[160:161], v[144:145], v[174:175]
	v_pk_add_f32 v[130:131], v[130:131], v[132:133]
	v_mfma_f32_16x16x32_bf16 v[142:145], v[232:235], v[2:5], v[204:207]
	v_add_f32_e64 v152, v152, v156
	v_add_f32_e64 v153, v153, v157
	v_pk_add_f32 v[156:157], v[158:159], v[160:161]
	v_pk_add_f32 v[158:159], v[134:135], v[136:137]
	v_mfma_f32_16x16x32_bf16 v[138:141], v[232:235], v[6:9], v[208:211]
	v_add_f32_e64 v150, v150, v130
	v_add_f32_e64 v151, v151, v131
	v_pk_add_f32 v[150:151], v[152:153], v[150:151]
	s_waitcnt lgkmcnt(0)
	v_mfma_f32_16x16x32_bf16 v[134:137], v[236:239], v[2:5], v[212:215]
	v_add_f32_e64 v150, v156, v150
	v_add_f32_e64 v151, v157, v151
	v_pk_add_f32 v[150:151], v[158:159], v[150:151]
	v_mfma_f32_16x16x32_bf16 v[196:199], v[224:227], v[2:5], v[196:199]
	v_mfma_f32_16x16x32_bf16 v[224:227], v[228:231], v[2:5], v[146:149]
	v_mfma_f32_16x16x32_bf16 v[146:149], v[228:231], v[6:9], v[200:203]
	v_mfma_f32_16x16x32_bf16 v[130:133], v[236:239], v[6:9], v[216:219]
	ds_read_b64_tr_b16 v[156:157], v189 offset:0
	ds_read_b64_tr_b16 v[158:159], v189 offset:0x200
	ds_read_b64_tr_b16 v[164:165], v189 offset:0x400
	ds_read_b64_tr_b16 v[166:167], v189 offset:0x600
	ds_read_b64_tr_b16 v[168:169], v189 offset:0x820
	ds_read_b64_tr_b16 v[170:171], v189 offset:0xa20
	ds_read_b64_tr_b16 v[172:173], v189 offset:0xc20
	ds_read_b64_tr_b16 v[174:175], v189 offset:0xe20
	ds_read_b64_tr_b16 v[200:201], v189 offset:0x1040
	ds_read_b64_tr_b16 v[202:203], v189 offset:0x1240
	ds_read_b64_tr_b16 v[204:205], v189 offset:0x1440
	ds_read_b64_tr_b16 v[206:207], v189 offset:0x1640
	s_waitcnt lgkmcnt(4)
; template <int D0> __device__ __forceinline__ void pv16(f32x4a (&o)[8][2], int vb, const bf16x8 (&pb)[2][2]) {
;     ...
;   const s16x4 a0 = TR(D0, 0, 0), a1 = TR(D0, 0, 1), a2 = TR(D0, 1, 0), a3 = TR(D0, 1, 1), b0 = TR(D0 + 1, 0, 0), b1 = TR(D0 + 1, 0, 1), b2 = TR(D0 + 1, 1, 0), b3 = TR(D0 + 1, 1, 1);
;   const s16x4 c0 = TR(D0 + 2, 0, 0), c1 = TR(D0 + 2, 0, 1), c2 = TR(D0 + 2, 1, 0), c3 = TR(D0 + 2, 1, 1);
;   asm volatile("s_waitcnt lgkmcnt(4)" ::: "memory"); SBAR();
;   o[D0][0] = MFMA16(PK16(a0, a1), pb[0][0], o[D0][0]); o[D0][1] = MFMA16(PK16(a0, a1), pb[0][1], o[D0][1]);
;   o[D0 + 1][0] = MFMA16(PK16(b0, b1), pb[0][0], o[D0 + 1][0]); o[D0 + 1][1] = MFMA16(PK16(b0, b1), pb[0][1], o[D0 + 1][1]);
;   o[D0][0] = MFMA16(PK16(a2, a3), pb[1][0], o[D0][0]); o[D0][1] = MFMA16(PK16(a2, a3), pb[1][1], o[D0][1]);
;   o[D0 + 1][0] = MFMA16(PK16(b2, b3), pb[1][0], o[D0 + 1][0]); o[D0 + 1][1] = MFMA16(PK16(b2, b3), pb[1][1], o[D0 + 1][1]);
;   SBAR();
;   const s16x4 d0 = TR(D0 + 3, 0, 0), d1 = TR(D0 + 3, 0, 1), d2 = TR(D0 + 3, 1, 0), d3 = TR(D0 + 3, 1, 1);
;   asm volatile("s_waitcnt lgkmcnt(4)" ::: "memory"); SBAR();
;   o[D0 + 2][0] = MFMA16(PK16(c0, c1), pb[0][0], o[D0 + 2][0]); o[D0 + 2][1] = MFMA16(PK16(c0, c1), pb[0][1], o[D0 + 2][1]);
;   o[D0 + 2][0] = MFMA16(PK16(c2, c3), pb[1][0], o[D0 + 2][0]); o[D0 + 2][1] = MFMA16(PK16(c2, c3), pb[1][1], o[D0 + 2][1]);
;   asm volatile("s_waitcnt lgkmcnt(0)" ::: "memory"); SBAR();
;   o[D0 + 3][0] = MFMA16(PK16(d0, d1), pb[0][0], o[D0 + 3][0]); o[D0 + 3][1] = MFMA16(PK16(d0, d1), pb[0][1], o[D0 + 3][1]);
;   o[D0 + 3][0] = MFMA16(PK16(d2, d3), pb[1][0], o[D0 + 3][0]); o[D0 + 3][1] = MFMA16(PK16(d2, d3), pb[1][1], o[D0 + 3][1]);
; template <int LDQ, int LDK, int LDO>
; __device__ __forceinline__ void attn_gqa16_body(const bf16* __restrict__ Qb, const bf16* __restrict__ Kh, const bf16* __restrict__ Vh, bf16* __restrict__ Ob, int seq, char* lds, float mref) {
;     ...
;     HPACK();
;     __syncthreads();
;     const bool more = t + 1 < NT;
;     if (more) HQK((t + 1) & 1);
;     const int vb = vb0 + (t & 1) * (int)G16_V;
;     SBAR(); pv16<0>(o, vb, pb); SBAR();
;     asm volatile("s_waitcnt vmcnt(0)" ::: "memory");
;     if (t + 2 < NT) HWRITEK(t & 1);
;     if (t + 1 < NT) HWRITEV((t + 1) & 1);
;     HLOADK(t + 3); HLOADV(t + 2);
;     SBAR(); pv16<4>(o, vb, pb); SBAR();
;     if (more) HEXP();
	s_nop 0
	v_mfma_f32_16x16x32_bf16 v[102:105], v[156:159], v[114:117], v[102:105]
	v_mfma_f32_16x16x32_bf16 v[98:101], v[156:159], v[118:121], v[98:101]
	v_mfma_f32_16x16x32_bf16 v[94:97], v[168:171], v[114:117], v[94:97]
	v_exp_f32_e32 v246, v196
	v_mfma_f32_16x16x32_bf16 v[90:93], v[168:171], v[118:121], v[90:93]
	v_exp_f32_e32 v240, v198
	v_mfma_f32_16x16x32_bf16 v[102:105], v[164:167], v[122:125], v[102:105]
	v_exp_f32_e32 v160, v199
	v_mfma_f32_16x16x32_bf16 v[98:101], v[164:167], v[126:129], v[98:101]
	v_exp_f32_e32 v247, v220
	v_mfma_f32_16x16x32_bf16 v[94:97], v[172:175], v[122:125], v[94:97]
	v_exp_f32_e32 v241, v222
	v_mfma_f32_16x16x32_bf16 v[90:93], v[172:175], v[126:129], v[90:93]
	v_exp_f32_e32 v161, v223
	ds_read_b64_tr_b16 v[156:157], v189 offset:0x1860
	ds_read_b64_tr_b16 v[158:159], v189 offset:0x1a60
	ds_read_b64_tr_b16 v[164:165], v189 offset:0x1c60
	ds_read_b64_tr_b16 v[166:167], v189 offset:0x1e60
	s_waitcnt lgkmcnt(4)
	v_mfma_f32_16x16x32_bf16 v[78:81], v[200:203], v[114:117], v[78:81]
	v_exp_f32_e32 v172, v143
	s_waitcnt lgkmcnt(0)
	v_mfma_f32_16x16x32_bf16 v[50:53], v[200:203], v[118:121], v[50:53]
	v_exp_f32_e32 v174, v145
	v_mfma_f32_16x16x32_bf16 v[78:81], v[204:207], v[122:125], v[78:81]
	v_exp_f32_e32 v143, v138
	v_mfma_f32_16x16x32_bf16 v[50:53], v[204:207], v[126:129], v[50:53]
	v_exp_f32_e32 v173, v139
	v_mfma_f32_16x16x32_bf16 v[82:85], v[156:159], v[114:117], v[82:85]
	v_exp_f32_e32 v145, v140
	v_mfma_f32_16x16x32_bf16 v[86:89], v[156:159], v[118:121], v[86:89]
	v_exp_f32_e32 v175, v141
	v_mfma_f32_16x16x32_bf16 v[82:85], v[164:167], v[122:125], v[82:85]
	v_exp_f32_e32 v138, v135
	v_mfma_f32_16x16x32_bf16 v[86:89], v[164:167], v[126:129], v[86:89]
	v_exp_f32_e32 v140, v137
	v_lshl_add_u64 v[152:153], v[162:163], 0, s[14:15]
	v_add_co_u32_e32 v156, vcc, s37, v152
	s_mulk_i32 s16, 0x4400
	s_nop 0
	v_addc_co_u32_e32 v157, vcc, 0, v153, vcc
	v_add_co_u32_e32 v158, vcc, s38, v152
	v_add_u32_e32 v164, s16, v194
	s_nop 0
	v_addc_co_u32_e32 v159, vcc, 0, v153, vcc
	s_waitcnt vmcnt(2)
	ds_write_b128 v164, v[106:109] offset:33280
	ds_write_b128 v164, v[110:113] offset:41984
	global_load_dwordx4 v[106:109], v[156:157], off offset:3072
	global_load_dwordx4 v[110:113], v[158:159], off offset:3072
	ds_read_b64_tr_b16 v[156:157], v189 offset:0x2080
	ds_read_b64_tr_b16 v[158:159], v189 offset:0x2280
	ds_read_b64_tr_b16 v[164:165], v189 offset:0x2480
	ds_read_b64_tr_b16 v[166:167], v189 offset:0x2680
	ds_read_b64_tr_b16 v[200:201], v189 offset:0x28a0
	ds_read_b64_tr_b16 v[202:203], v189 offset:0x2aa0
	ds_read_b64_tr_b16 v[204:205], v189 offset:0x2ca0
	ds_read_b64_tr_b16 v[206:207], v189 offset:0x2ea0
	s_waitcnt lgkmcnt(6)
	s_nop 0
	v_mfma_f32_16x16x32_bf16 v[54:57], v[156:159], v[114:117], v[54:57]
	v_exp_f32_e32 v135, v130
	v_mfma_f32_16x16x32_bf16 v[62:65], v[156:159], v[118:121], v[62:65]
	v_exp_f32_e32 v139, v131
	ds_read_b64_tr_b16 v[156:157], v189 offset:0x30c0
	ds_read_b64_tr_b16 v[158:159], v189 offset:0x32c0
	s_waitcnt lgkmcnt(4)
	v_mfma_f32_16x16x32_bf16 v[58:61], v[200:203], v[114:117], v[58:61]
	v_exp_f32_e32 v137, v132
	v_mfma_f32_16x16x32_bf16 v[70:73], v[200:203], v[118:121], v[70:73]
	v_exp_f32_e32 v141, v133
	ds_read_b64_tr_b16 v[200:201], v189 offset:0x38e0
	ds_read_b64_tr_b16 v[202:203], v189 offset:0x3ae0
	s_waitcnt lgkmcnt(6)
	v_mfma_f32_16x16x32_bf16 v[54:57], v[164:167], v[122:125], v[54:57]
	v_exp_f32_e32 v168, v224
	v_mfma_f32_16x16x32_bf16 v[62:65], v[164:167], v[126:129], v[62:65]
	v_exp_f32_e32 v170, v225
	ds_read_b64_tr_b16 v[164:165], v189 offset:0x34c0
	ds_read_b64_tr_b16 v[166:167], v189 offset:0x36c0
	s_waitcnt lgkmcnt(6)
	v_mfma_f32_16x16x32_bf16 v[58:61], v[204:207], v[122:125], v[58:61]
	v_exp_f32_e32 v169, v146
	v_mfma_f32_16x16x32_bf16 v[70:73], v[204:207], v[126:129], v[70:73]
	v_exp_f32_e32 v171, v147
	ds_read_b64_tr_b16 v[204:205], v189 offset:0x3ce0
	ds_read_b64_tr_b16 v[206:207], v189 offset:0x3ee0
	s_waitcnt lgkmcnt(6)
	v_mfma_f32_16x16x32_bf16 v[42:45], v[156:159], v[114:117], v[42:45]
	v_exp_f32_e32 v152, v197
	v_exp_f32_e32 v134, v134
	v_mfma_f32_16x16x32_bf16 v[46:49], v[156:159], v[118:121], v[46:49]
	v_exp_f32_e32 v153, v221
	v_exp_f32_e32 v136, v136
	s_waitcnt lgkmcnt(4)
	v_mfma_f32_16x16x32_bf16 v[66:69], v[200:203], v[114:117], v[66:69]
	v_exp_f32_e32 v242, v226
	v_mfma_f32_16x16x32_bf16 v[74:77], v[200:203], v[118:121], v[74:77]
	v_exp_f32_e32 v244, v227
	s_waitcnt lgkmcnt(2)
	v_mfma_f32_16x16x32_bf16 v[42:45], v[164:167], v[122:125], v[42:45]
	v_exp_f32_e32 v243, v148
	v_mfma_f32_16x16x32_bf16 v[46:49], v[164:167], v[126:129], v[46:49]
	v_exp_f32_e32 v245, v149
	s_waitcnt lgkmcnt(0)
	v_mfma_f32_16x16x32_bf16 v[66:69], v[204:207], v[122:125], v[66:69]
	v_exp_f32_e32 v142, v142
	v_mfma_f32_16x16x32_bf16 v[74:77], v[204:207], v[126:129], v[74:77]
	v_exp_f32_e32 v144, v144
	s_add_u32 s14, s14, 0x90000
	s_addc_u32 s15, s15, 0
	s_cmp_lg_u32 s14, 0x9120000
	s_mov_b32 s16, s17
	s_cbranch_scc1 .LBB0_650
	v_mov_b32_e32 v156, v240
	v_mov_b32_e32 v157, v241
	v_mov_b32_e32 v158, v246
	v_mov_b32_e32 v159, v247
	v_mov_b32_e32 v164, v242
	v_mov_b32_e32 v165, v243
	v_mov_b32_e32 v166, v244
	v_mov_b32_e32 v167, v245
	s_waitcnt vmcnt(1)
	v_cvt_pk_bf16_f32 v106, v158, v152
	v_cvt_pk_bf16_f32 v107, v156, v160
	v_cvt_pk_bf16_f32 v108, v168, v170
	v_cvt_pk_bf16_f32 v109, v164, v166
	s_waitcnt vmcnt(0)
	v_cvt_pk_bf16_f32 v110, v159, v153
	v_cvt_pk_bf16_f32 v111, v157, v161
	v_cvt_pk_bf16_f32 v112, v169, v171
	v_cvt_pk_bf16_f32 v113, v165, v167
	v_cvt_pk_bf16_f32 v114, v142, v172
	v_cvt_pk_bf16_f32 v115, v144, v174
	v_cvt_pk_bf16_f32 v116, v134, v138
	v_cvt_pk_bf16_f32 v117, v136, v140
	v_cvt_pk_bf16_f32 v118, v143, v173
	v_cvt_pk_bf16_f32 v119, v145, v175
	v_cvt_pk_bf16_f32 v120, v135, v139
	v_cvt_pk_bf16_f32 v121, v137, v141
	s_waitcnt lgkmcnt(0)
	s_barrier
; #define SBAR() __builtin_amdgcn_sched_barrier(0)
; #define HLOADV(kt) do { const char* vb_ = (const char*)Vh + (size_t)(kt) * (64 * LDK * 2); sv0 = *(const bf16x8*)(vb_ + koff0); sv1 = *(const bf16x8*)(vb_ + koff1); } while (0)
; #define HLOADK(kt) do { const char* kb_ = (const char*)Kh + (size_t)(kt) * (64 * LDK * 2); sk0 = *(const bf16x8*)(kb_ + koff0); sk1 = *(const bf16x8*)(kb_ + koff1); } while (0)
; #define HWRITEV(b) do { char* d_ = V_lds + (b) * G16_V; *(bf16x8*)(d_ + vst0) = sv0; *(bf16x8*)(d_ + vst1) = sv1; } while (0)
; #define HWRITEK(b) do { char* d_ = K_lds + (b) * GB_K; *(bf16x8*)(d_ + KSWZ(sr, sc * 2)) = sk0; *(bf16x8*)(d_ + KSWZ(32 + sr, sc * 2)) = sk1; } while (0)
; template <int LDQ, int LDK, int LDO>
; __device__ __forceinline__ void attn_gqa16_body(const bf16* __restrict__ Qb, const bf16* __restrict__ Kh, const bf16* __restrict__ Vh, bf16* __restrict__ Ob, int seq, char* lds, float mref) {
;     ...
;     HPACK();
;     __syncthreads();
;     const bool more = t + 1 < NT;
;     if (more) HQK((t + 1) & 1);
;     const int vb = vb0 + (t & 1) * (int)G16_V;
;     SBAR(); pv16<0>(o, vb, pb); SBAR();
;     asm volatile("s_waitcnt vmcnt(0)" ::: "memory");
;     if (t + 2 < NT) HWRITEK(t & 1);
;     if (t + 1 < NT) HWRITEV((t + 1) & 1);
;     HLOADK(t + 3); HLOADV(t + 2);
;     SBAR(); pv16<4>(o, vb, pb); SBAR();
	s_mov_b32 m0, s86
	s_nop 0
	global_load_lds_dwordx4 v253, s[74:75]
	s_add_i32 m0, s86, 0x400
	s_nop 0
	global_load_lds_dwordx4 v253, s[76:77]
	ds_read_b128 v[122:125], v182 offset:50688
	ds_read_b128 v[126:129], v182 offset:50752
	ds_read_b128 v[146:149], v182 offset:55040
	ds_read_b128 v[196:199], v182 offset:55104
	ds_read_b128 v[204:207], v182 offset:59392
	ds_read_b128 v[208:211], v182 offset:59456
	ds_read_b128 v[216:219], v182 offset:63744
	ds_read_b128 v[220:223], v182 offset:63808
	s_waitcnt lgkmcnt(7)
	v_mfma_f32_16x16x32_bf16 v[130:133], v[122:125], v[30:33], 0
	v_mov_b32_e32 v190, v168
	v_mov_b32_e32 v191, v158
	v_mov_b32_e32 v192, v170
	v_mfma_f32_16x16x32_bf16 v[122:125], v[122:125], v[38:41], 0
	v_mov_b32_e32 v193, v152
	v_mov_b32_e32 v152, v171
	s_lshl_b32 s8, s8, 12
	s_waitcnt lgkmcnt(5)
	v_mfma_f32_16x16x32_bf16 v[200:203], v[146:149], v[30:33], 0
	s_add_u32 s8, s42, s8
	s_addc_u32 s14, s43, 0
	s_add_u32 s12, s8, s12
	v_mfma_f32_16x16x32_bf16 v[146:149], v[146:149], v[38:41], 0
	s_addc_u32 s13, s14, s13
	s_waitcnt lgkmcnt(3)
	v_mfma_f32_16x16x32_bf16 v[212:215], v[204:207], v[30:33], 0
	s_waitcnt lgkmcnt(1)
	v_mfma_f32_16x16x32_bf16 v[30:33], v[216:219], v[30:33], 0
	v_mfma_f32_16x16x32_bf16 v[130:133], v[126:129], v[18:21], v[130:133]
	v_mfma_f32_16x16x32_bf16 v[122:125], v[126:129], v[22:25], v[122:125]
	v_mfma_f32_16x16x32_bf16 v[126:129], v[196:199], v[18:21], v[200:203]
	v_mfma_f32_16x16x32_bf16 v[146:149], v[196:199], v[22:25], v[146:149]
	v_mfma_f32_16x16x32_bf16 v[196:199], v[208:211], v[18:21], v[212:215]
	s_waitcnt lgkmcnt(0)
	v_mfma_f32_16x16x32_bf16 v[18:21], v[220:223], v[18:21], v[30:33]
	s_nop 0
	v_mov_b32_e32 v213, v156
	v_mov_b32_e32 v212, v164
	v_mov_b32_e32 v214, v166
	ds_read_b128 v[30:33], v182 offset:50816
	v_mfma_f32_16x16x32_bf16 v[204:207], v[204:207], v[38:41], 0
	v_mov_b32_e32 v215, v160
	v_mfma_f32_16x16x32_bf16 v[38:41], v[216:219], v[38:41], 0
	v_mov_b32_e32 v216, v169
	v_mov_b32_e32 v217, v159
	v_mov_b32_e32 v219, v157
	v_mfma_f32_16x16x32_bf16 v[200:203], v[208:211], v[22:25], v[204:207]
	v_mov_b32_e32 v218, v165
	v_mfma_f32_16x16x32_bf16 v[22:25], v[220:223], v[22:25], v[38:41]
	s_nop 2
	ds_read_b128 v[38:41], v182 offset:55168
	ds_read_b128 v[204:207], v182 offset:50880
	s_waitcnt lgkmcnt(2)
	v_mfma_f32_16x16x32_bf16 v[130:133], v[30:33], v[10:13], v[130:133]
	v_mfma_f32_16x16x32_bf16 v[30:33], v[30:33], v[14:17], v[122:125]
	s_nop 2
	ds_read_b128 v[122:125], v182 offset:59520
	ds_read_b128 v[208:211], v182 offset:55232
	s_waitcnt lgkmcnt(3)
	v_mfma_f32_16x16x32_bf16 v[126:129], v[38:41], v[10:13], v[126:129]
	v_mfma_f32_16x16x32_bf16 v[38:41], v[38:41], v[14:17], v[146:149]
	s_nop 2
	ds_read_b128 v[146:149], v182 offset:63872
	ds_read_b128 v[168:171], v182 offset:59584
	ds_read_b128 v[156:159], v182 offset:63936
	s_waitcnt lgkmcnt(4)
	v_mfma_f32_16x16x32_bf16 v[196:199], v[122:125], v[10:13], v[196:199]
	s_waitcnt lgkmcnt(2)
	v_mfma_f32_16x16x32_bf16 v[10:13], v[146:149], v[10:13], v[18:21]
	v_mfma_f32_16x16x32_bf16 v[122:125], v[122:125], v[14:17], v[200:203]
	s_nop 1
	v_mov_b32_e32 v18, v142
	v_mov_b32_e32 v19, v144
	v_mov_b32_e32 v20, v172
	v_mfma_f32_16x16x32_bf16 v[14:17], v[146:149], v[14:17], v[22:25]
	v_mov_b32_e32 v201, v161
	v_mov_b32_e32 v200, v167
	v_mov_b32_e32 v21, v174
	v_mfma_f32_16x16x32_bf16 v[160:163], v[204:207], v[6:9], v[30:33]
	v_add_f32_e64 v24, v190, v192
	v_add_f32_e64 v25, v191, v193
	v_mov_b32_e32 v144, v143
	v_mov_b32_e32 v22, v173
	v_pk_add_f32 v[30:31], v[212:213], v[214:215]
	v_mfma_f32_16x16x32_bf16 v[146:149], v[204:207], v[2:5], v[130:133]
	v_add_f32_e64 v24, v24, v30
	v_add_f32_e64 v25, v25, v31
	v_mov_b32_e32 v23, v175
	v_pk_add_f32 v[32:33], v[216:217], v[152:153]
	v_mfma_f32_16x16x32_bf16 v[164:167], v[208:211], v[2:5], v[126:129]
	v_add_f32_e64 v144, v144, v22
	v_add_f32_e64 v145, v145, v23
	v_add_f32_e32 v130, v134, v138
	v_add_f32_e32 v132, v136, v140
	v_mfma_f32_16x16x32_bf16 v[172:175], v[208:211], v[6:9], v[38:41]
	v_add_f32_e64 v126, v18, v20
	v_add_f32_e64 v127, v19, v21
	s_nop 0
	v_pk_add_f32 v[38:39], v[218:219], v[200:201]
	s_waitcnt lgkmcnt(1)
	v_mfma_f32_16x16x32_bf16 v[196:199], v[168:171], v[2:5], v[196:199]
	v_add_f32_e64 v142, v32, v38
	v_add_f32_e64 v143, v33, v39
	s_waitcnt lgkmcnt(0)
	v_mfma_f32_16x16x32_bf16 v[200:203], v[156:159], v[2:5], v[10:13]
	v_add_f32_e64 v2, v150, v25
	v_add_f32_e64 v3, v151, v24
	v_pk_add_f32 v[128:129], v[24:25], v[2:3]
	v_mfma_f32_16x16x32_bf16 v[168:171], v[168:171], v[6:9], v[122:125]
	s_nop 2
	v_add_f32_e32 v122, v135, v139
	v_add_f32_e32 v124, v137, v141
	v_mfma_f32_16x16x32_bf16 v[134:137], v[156:159], v[6:9], v[14:17]
	ds_read_b64_tr_b16 v[2:3], v183 offset:0
	ds_read_b64_tr_b16 v[4:5], v183 offset:0x200
	ds_read_b64_tr_b16 v[6:7], v183 offset:0x400
	ds_read_b64_tr_b16 v[8:9], v183 offset:0x600
	ds_read_b64_tr_b16 v[10:11], v183 offset:0x820
	ds_read_b64_tr_b16 v[12:13], v183 offset:0xa20
	ds_read_b64_tr_b16 v[14:15], v183 offset:0xc20
	ds_read_b64_tr_b16 v[16:17], v183 offset:0xe20
	ds_read_b64_tr_b16 v[18:19], v183 offset:0x1040
	ds_read_b64_tr_b16 v[20:21], v183 offset:0x1240
	ds_read_b64_tr_b16 v[22:23], v183 offset:0x1440
	ds_read_b64_tr_b16 v[24:25], v183 offset:0x1640
	s_waitcnt lgkmcnt(4)
	s_nop 0
	v_mfma_f32_16x16x32_bf16 v[30:33], v[2:5], v[106:109], v[102:105]
	v_mfma_f32_16x16x32_bf16 v[38:41], v[2:5], v[110:113], v[98:101]
	v_mfma_f32_16x16x32_bf16 v[94:97], v[10:13], v[106:109], v[94:97]
	v_mfma_f32_16x16x32_bf16 v[10:13], v[10:13], v[110:113], v[90:93]
	v_mfma_f32_16x16x32_bf16 v[2:5], v[6:9], v[114:117], v[30:33]
	v_mfma_f32_16x16x32_bf16 v[6:9], v[6:9], v[118:121], v[38:41]
	v_mfma_f32_16x16x32_bf16 v[38:41], v[14:17], v[114:117], v[94:97]
	v_mfma_f32_16x16x32_bf16 v[90:93], v[14:17], v[118:121], v[10:13]
	ds_read_b64_tr_b16 v[14:15], v183 offset:0x1860
	ds_read_b64_tr_b16 v[16:17], v183 offset:0x1a60
	ds_read_b64_tr_b16 v[30:31], v183 offset:0x1c60
	ds_read_b64_tr_b16 v[32:33], v183 offset:0x1e60
	s_waitcnt lgkmcnt(4)
; #define SBAR() __builtin_amdgcn_sched_barrier(0)
; #define HLOADV(kt) do { const char* vb_ = (const char*)Vh + (size_t)(kt) * (64 * LDK * 2); sv0 = *(const bf16x8*)(vb_ + koff0); sv1 = *(const bf16x8*)(vb_ + koff1); } while (0)
; #define HLOADK(kt) do { const char* kb_ = (const char*)Kh + (size_t)(kt) * (64 * LDK * 2); sk0 = *(const bf16x8*)(kb_ + koff0); sk1 = *(const bf16x8*)(kb_ + koff1); } while (0)
; #define HWRITEV(b) do { char* d_ = V_lds + (b) * G16_V; *(bf16x8*)(d_ + vst0) = sv0; *(bf16x8*)(d_ + vst1) = sv1; } while (0)
; #define HWRITEK(b) do { char* d_ = K_lds + (b) * GB_K; *(bf16x8*)(d_ + KSWZ(sr, sc * 2)) = sk0; *(bf16x8*)(d_ + KSWZ(32 + sr, sc * 2)) = sk1; } while (0)
; #define HEXP() do { _Pragma("unroll") for (int kt = 0; kt < 4; ++kt) { _Pragma("unroll") for (int qt = 0; qt < 2; ++qt) { _Pragma("unroll") for (int i = 0; i < 4; ++i) s[kt][qt][i] = __builtin_amdgcn_exp2f(fmaf(s[kt][qt][i], C, mnC)); } } } while (0)
; template <int LDQ, int LDK, int LDO>
; __device__ __forceinline__ void attn_gqa16_body(const bf16* __restrict__ Qb, const bf16* __restrict__ Kh, const bf16* __restrict__ Vh, bf16* __restrict__ Ob, int seq, char* lds, float mref) {
;     ...
;     SBAR(); pv16<0>(o, vb, pb); SBAR();
;     asm volatile("s_waitcnt vmcnt(0)" ::: "memory");
;     if (t + 2 < NT) HWRITEK(t & 1);
;     if (t + 1 < NT) HWRITEV((t + 1) & 1);
;     HLOADK(t + 3); HLOADV(t + 2);
;     SBAR(); pv16<4>(o, vb, pb); SBAR();
;     if (more) HEXP();
	v_mfma_f32_16x16x32_bf16 v[10:13], v[18:21], v[106:109], v[78:81]
	s_waitcnt lgkmcnt(0)
	v_mfma_f32_16x16x32_bf16 v[18:21], v[18:21], v[110:113], v[50:53]
	v_mfma_f32_16x16x32_bf16 v[10:13], v[22:25], v[114:117], v[10:13]
	v_mfma_f32_16x16x32_bf16 v[22:25], v[22:25], v[118:121], v[18:21]
	v_mfma_f32_16x16x32_bf16 v[18:21], v[14:17], v[106:109], v[82:85]
	v_mfma_f32_16x16x32_bf16 v[50:53], v[14:17], v[110:113], v[86:89]
	v_mfma_f32_16x16x32_bf16 v[14:17], v[30:33], v[114:117], v[18:21]
	v_mfma_f32_16x16x32_bf16 v[18:21], v[30:33], v[118:121], v[50:53]
	s_waitcnt vmcnt(0)
	s_waitcnt vmcnt(1)
	s_waitcnt vmcnt(0)
	ds_read_b64_tr_b16 v[26:27], v183 offset:0x2080
	ds_read_b64_tr_b16 v[28:29], v183 offset:0x2280
	ds_read_b64_tr_b16 v[30:31], v183 offset:0x2480
	ds_read_b64_tr_b16 v[32:33], v183 offset:0x2680
	ds_read_b64_tr_b16 v[34:35], v183 offset:0x28a0
	ds_read_b64_tr_b16 v[36:37], v183 offset:0x2aa0
	ds_read_b64_tr_b16 v[78:79], v183 offset:0x2ca0
	ds_read_b64_tr_b16 v[80:81], v183 offset:0x2ea0
	ds_read_b64_tr_b16 v[82:83], v183 offset:0x30c0
	ds_read_b64_tr_b16 v[84:85], v183 offset:0x32c0
	ds_read_b64_tr_b16 v[86:87], v183 offset:0x34c0
	ds_read_b64_tr_b16 v[88:89], v183 offset:0x36c0
	s_waitcnt lgkmcnt(4)
	s_nop 0
	v_mfma_f32_16x16x32_bf16 v[50:53], v[26:29], v[106:109], v[54:57]
	v_mfma_f32_16x16x32_bf16 v[26:29], v[26:29], v[110:113], v[62:65]
	v_mfma_f32_16x16x32_bf16 v[58:61], v[34:37], v[106:109], v[58:61]
	v_mfma_f32_16x16x32_bf16 v[34:37], v[34:37], v[110:113], v[70:73]
	v_mfma_f32_16x16x32_bf16 v[50:53], v[30:33], v[114:117], v[50:53]
	v_mfma_f32_16x16x32_bf16 v[54:57], v[30:33], v[118:121], v[26:29]
	v_mfma_f32_16x16x32_bf16 v[70:73], v[78:81], v[114:117], v[58:61]
	v_mfma_f32_16x16x32_bf16 v[78:81], v[78:81], v[118:121], v[34:37]
	ds_read_b64_tr_b16 v[30:31], v183 offset:0x38e0
	ds_read_b64_tr_b16 v[32:33], v183 offset:0x3ae0
	ds_read_b64_tr_b16 v[34:35], v183 offset:0x3ce0
	ds_read_b64_tr_b16 v[36:37], v183 offset:0x3ee0
	s_waitcnt lgkmcnt(4)
	v_mfma_f32_16x16x32_bf16 v[26:29], v[82:85], v[106:109], v[42:45]
	s_waitcnt lgkmcnt(0)
	v_mfma_f32_16x16x32_bf16 v[42:45], v[82:85], v[110:113], v[46:49]
	v_mfma_f32_16x16x32_bf16 v[26:29], v[86:89], v[114:117], v[26:29]
	v_mfma_f32_16x16x32_bf16 v[58:61], v[86:89], v[118:121], v[42:45]
	v_mfma_f32_16x16x32_bf16 v[42:45], v[30:33], v[106:109], v[66:69]
	v_mfma_f32_16x16x32_bf16 v[46:49], v[30:33], v[110:113], v[74:77]
	v_mfma_f32_16x16x32_bf16 v[30:33], v[34:37], v[114:117], v[42:45]
	v_mfma_f32_16x16x32_bf16 v[62:65], v[34:37], v[118:121], v[46:49]
	s_nop 4
	v_add_f32_e32 v42, v186, v196
	v_exp_f32_e32 v116, v42
	v_add_f32_e32 v42, v186, v197
	v_exp_f32_e32 v117, v42
	v_add_f32_e32 v42, v186, v198
	v_exp_f32_e32 v118, v42
	v_add_f32_e32 v42, v186, v199
	v_exp_f32_e32 v119, v42
	v_add_f32_e32 v42, v186, v168
	v_add_f32_e32 v34, v186, v146
	v_exp_f32_e32 v98, v42
	v_add_f32_e32 v42, v186, v169
	v_exp_f32_e32 v131, v34
	v_add_f32_e32 v34, v186, v147
	v_exp_f32_e32 v99, v42
	v_add_f32_e32 v42, v186, v170
	v_exp_f32_e32 v133, v34
	v_add_f32_e32 v34, v186, v148
	v_exp_f32_e32 v100, v42
	v_add_f32_e32 v42, v186, v171
	v_exp_f32_e32 v74, v34
	v_add_f32_e32 v34, v186, v149
	v_exp_f32_e32 v101, v42
	v_add_f32_e32 v42, v186, v200
	v_exp_f32_e32 v129, v34
	v_add_f32_e32 v34, v186, v160
	v_exp_f32_e32 v120, v42
	v_add_f32_e32 v42, v186, v201
	v_exp_f32_e32 v123, v34
	v_add_f32_e32 v34, v186, v161
	v_exp_f32_e32 v121, v42
	v_add_f32_e32 v42, v186, v202
	v_exp_f32_e32 v125, v34
	v_add_f32_e32 v34, v186, v162
	v_exp_f32_e32 v75, v42
	v_add_f32_e32 v42, v186, v203
	v_exp_f32_e32 v76, v34
	v_add_f32_e32 v34, v186, v163
	v_exp_f32_e32 v77, v42
	v_add_f32_e32 v42, v186, v134
	v_exp_f32_e32 v87, v34
	v_add_f32_e32 v34, v186, v164
	v_exp_f32_e32 v102, v42
	v_add_f32_e32 v42, v186, v135
	v_exp_f32_e32 v66, v34
	v_add_f32_e32 v34, v186, v165
	v_exp_f32_e32 v103, v42
	v_add_f32_e32 v42, v186, v136
	v_exp_f32_e32 v68, v34
	v_add_f32_e32 v34, v186, v166
	v_exp_f32_e32 v43, v42
	v_exp_f32_e32 v67, v34
	v_add_f32_e32 v34, v186, v167
	v_add_f32_e32 v35, v186, v173
	v_exp_f32_e32 v69, v34
	v_add_f32_e32 v34, v186, v172
	v_exp_f32_e32 v36, v35
	v_add_f32_e32 v35, v186, v174
	v_add_f32_e32 v37, v186, v175
	v_add_f32_e32 v42, v186, v137
	v_exp_f32_e32 v34, v34
	v_exp_f32_e32 v35, v35
	v_exp_f32_e32 v37, v37
	v_exp_f32_e32 v45, v42
	v_add_f32_e32 v42, v143, v151
	v_pk_add_f32 v[48:49], v[144:145], v[144:145] op_sel:[0,1] op_sel_hi:[1,0]
	v_pk_add_f32 v[84:85], v[142:143], v[42:43] op_sel_hi:[1,0]
	v_mov_b32_e32 v49, v76
	v_mov_b32_e32 v85, v87
	v_pk_add_f32 v[46:47], v[122:123], v[124:125]
	v_pk_add_f32 v[48:49], v[48:49], v[84:85]
	v_add_f32_e32 v42, v98, v99
	v_pk_add_f32 v[46:47], v[46:47], v[48:49]
	v_pk_add_f32 v[48:49], v[34:35], v[36:37]
	v_pk_add_f32 v[46:47], v[46:47], v[46:47] op_sel:[0,1] op_sel_hi:[1,0]
	v_pk_add_f32 v[48:49], v[48:49], v[48:49] op_sel:[0,1] op_sel_hi:[1,0]
	v_add_f32_e32 v44, v100, v101
	v_mov_b32_e32 v47, v102
	v_mov_b32_e32 v49, v103
	v_pk_add_f32 v[46:47], v[46:47], v[48:49]
	v_pk_add_f32 v[48:49], v[42:43], v[44:45]
	v_cvt_pk_bf16_f32 v82, v131, v133
	v_cvt_pk_bf16_f32 v83, v74, v129
	v_cvt_pk_bf16_f32 v84, v66, v68
	v_cvt_pk_bf16_f32 v85, v67, v69
	v_cvt_pk_bf16_f32 v86, v123, v125
	s_nop 0
	v_pk_add_f32 v[46:47], v[46:47], v[48:49]
	v_pk_add_f32 v[48:49], v[126:127], v[126:127] op_sel:[0,1] op_sel_hi:[1,0]
	v_add_f32_e32 v122, v46, v47
	v_mov_b32_e32 v49, v74
	v_pk_add_f32 v[46:47], v[130:131], v[132:133]
	v_pk_add_f32 v[48:49], v[48:49], v[128:129]
	v_cvt_pk_bf16_f32 v87, v76, v87
	v_cvt_pk_bf16_f32 v88, v34, v36
	v_cvt_pk_bf16_f32 v89, v35, v37
	v_cvt_pk_bf16_f32 v94, v116, v117
	v_cvt_pk_bf16_f32 v95, v118, v119
	s_nop 0
	v_pk_add_f32 v[114:115], v[46:47], v[48:49]
	v_cvt_pk_bf16_f32 v96, v120, v121
	v_cvt_pk_bf16_f32 v97, v75, v77
	v_cvt_pk_bf16_f32 v98, v98, v99
	v_cvt_pk_bf16_f32 v99, v100, v101
	v_cvt_pk_bf16_f32 v100, v102, v103
	v_cvt_pk_bf16_f32 v101, v43, v45
	s_waitcnt lgkmcnt(0)
	s_barrier
; #define SBAR() __builtin_amdgcn_sched_barrier(0)
; #define MFMA16(a, b, c) __builtin_amdgcn_mfma_f32_16x16x32_bf16(a, b, c, 0, 0, 0)
; template <int D0> __device__ __forceinline__ void pv16(f32x4a (&o)[8][2], int vb, const bf16x8 (&pb)[2][2]) {
;     ...
;   const s16x4 a0 = TR(D0, 0, 0), a1 = TR(D0, 0, 1), a2 = TR(D0, 1, 0), a3 = TR(D0, 1, 1), b0 = TR(D0 + 1, 0, 0), b1 = TR(D0 + 1, 0, 1), b2 = TR(D0 + 1, 1, 0), b3 = TR(D0 + 1, 1, 1);
;   const s16x4 c0 = TR(D0 + 2, 0, 0), c1 = TR(D0 + 2, 0, 1), c2 = TR(D0 + 2, 1, 0), c3 = TR(D0 + 2, 1, 1);
;   asm volatile("s_waitcnt lgkmcnt(4)" ::: "memory"); SBAR();
;   o[D0][0] = MFMA16(PK16(a0, a1), pb[0][0], o[D0][0]); o[D0][1] = MFMA16(PK16(a0, a1), pb[0][1], o[D0][1]);
;   o[D0 + 1][0] = MFMA16(PK16(b0, b1), pb[0][0], o[D0 + 1][0]); o[D0 + 1][1] = MFMA16(PK16(b0, b1), pb[0][1], o[D0 + 1][1]);
;   o[D0][0] = MFMA16(PK16(a2, a3), pb[1][0], o[D0][0]); o[D0][1] = MFMA16(PK16(a2, a3), pb[1][1], o[D0][1]);
;   o[D0 + 1][0] = MFMA16(PK16(b2, b3), pb[1][0], o[D0 + 1][0]); o[D0 + 1][1] = MFMA16(PK16(b2, b3), pb[1][1], o[D0 + 1][1]);
;   SBAR();
;   const s16x4 d0 = TR(D0 + 3, 0, 0), d1 = TR(D0 + 3, 0, 1), d2 = TR(D0 + 3, 1, 0), d3 = TR(D0 + 3, 1, 1);
;   asm volatile("s_waitcnt lgkmcnt(4)" ::: "memory"); SBAR();
;   o[D0 + 2][0] = MFMA16(PK16(c0, c1), pb[0][0], o[D0 + 2][0]); o[D0 + 2][1] = MFMA16(PK16(c0, c1), pb[0][1], o[D0 + 2][1]);
;   o[D0 + 2][0] = MFMA16(PK16(c2, c3), pb[1][0], o[D0 + 2][0]); o[D0 + 2][1] = MFMA16(PK16(c2, c3), pb[1][1], o[D0 + 2][1]);
;   asm volatile("s_waitcnt lgkmcnt(0)" ::: "memory"); SBAR();
;   o[D0 + 3][0] = MFMA16(PK16(d0, d1), pb[0][0], o[D0 + 3][0]); o[D0 + 3][1] = MFMA16(PK16(d0, d1), pb[0][1], o[D0 + 3][1]);
;   o[D0 + 3][0] = MFMA16(PK16(d2, d3), pb[1][0], o[D0 + 3][0]); o[D0 + 3][1] = MFMA16(PK16(d2, d3), pb[1][1], o[D0 + 3][1]);
; template <int LDQ, int LDK, int LDO>
; __device__ __forceinline__ void attn_gqa16_body(const bf16* __restrict__ Qb, const bf16* __restrict__ Kh, const bf16* __restrict__ Vh, bf16* __restrict__ Ob, int seq, char* lds, float mref) {
;     ...
;     SBAR(); pv16<4>(o, vb, pb); SBAR();
;     if (more) HEXP();
;   }
;   __builtin_amdgcn_s_setprio(0);
;   ls0 += __shfl_xor(ls0, 16); ls0 += __shfl_xor(ls0, 32); ls1 += __shfl_xor(ls1, 16); ls1 += __shfl_xor(ls1, 32);
;   const float rl[2] = {__builtin_amdgcn_rcpf(ls0), __builtin_amdgcn_rcpf(ls1)};
	ds_read_b64_tr_b16 v[34:35], v184 offset:0
	ds_read_b64_tr_b16 v[36:37], v184 offset:0x200
	ds_read_b64_tr_b16 v[42:43], v184 offset:0x400
	ds_read_b64_tr_b16 v[44:45], v184 offset:0x600
	ds_read_b64_tr_b16 v[46:47], v184 offset:0x820
	ds_read_b64_tr_b16 v[48:49], v184 offset:0xa20
	ds_read_b64_tr_b16 v[102:103], v184 offset:0xc20
	ds_read_b64_tr_b16 v[104:105], v184 offset:0xe20
	ds_read_b64_tr_b16 v[106:107], v184 offset:0x1040
	ds_read_b64_tr_b16 v[108:109], v184 offset:0x1240
	ds_read_b64_tr_b16 v[110:111], v184 offset:0x1440
	ds_read_b64_tr_b16 v[112:113], v184 offset:0x1640
	s_waitcnt lgkmcnt(4)
	s_nop 0
	v_mfma_f32_16x16x32_bf16 v[2:5], v[34:37], v[82:85], v[2:5]
	v_mfma_f32_16x16x32_bf16 v[6:9], v[34:37], v[86:89], v[6:9]
	v_mfma_f32_16x16x32_bf16 v[34:37], v[46:49], v[82:85], v[38:41]
	v_mfma_f32_16x16x32_bf16 v[46:49], v[46:49], v[86:89], v[90:93]
	v_mfma_f32_16x16x32_bf16 v[38:41], v[42:45], v[94:97], v[2:5]
	v_mfma_f32_16x16x32_bf16 v[6:9], v[42:45], v[98:101], v[6:9]
	v_mfma_f32_16x16x32_bf16 v[34:37], v[102:105], v[94:97], v[34:37]
	v_mfma_f32_16x16x32_bf16 v[2:5], v[102:105], v[98:101], v[46:49]
	ds_read_b64_tr_b16 v[46:47], v184 offset:0x1860
	ds_read_b64_tr_b16 v[48:49], v184 offset:0x1a60
	ds_read_b64_tr_b16 v[90:91], v184 offset:0x1c60
	ds_read_b64_tr_b16 v[92:93], v184 offset:0x1e60
	s_waitcnt lgkmcnt(4)
	v_mfma_f32_16x16x32_bf16 v[10:13], v[106:109], v[82:85], v[10:13]
	s_waitcnt lgkmcnt(0)
	v_mfma_f32_16x16x32_bf16 v[22:25], v[106:109], v[86:89], v[22:25]
	v_mfma_f32_16x16x32_bf16 v[42:45], v[110:113], v[94:97], v[10:13]
	v_mfma_f32_16x16x32_bf16 v[10:13], v[110:113], v[98:101], v[22:25]
	v_mfma_f32_16x16x32_bf16 v[14:17], v[46:49], v[82:85], v[14:17]
	v_mfma_f32_16x16x32_bf16 v[18:21], v[46:49], v[86:89], v[18:21]
	v_mfma_f32_16x16x32_bf16 v[46:49], v[90:93], v[94:97], v[14:17]
	v_mfma_f32_16x16x32_bf16 v[14:17], v[90:93], v[98:101], v[18:21]
	s_waitcnt vmcnt(0)
	ds_read_b64_tr_b16 v[18:19], v184 offset:0x2080
	ds_read_b64_tr_b16 v[20:21], v184 offset:0x2280
	ds_read_b64_tr_b16 v[22:23], v184 offset:0x2480
	ds_read_b64_tr_b16 v[24:25], v184 offset:0x2680
	ds_read_b64_tr_b16 v[90:91], v184 offset:0x28a0
	ds_read_b64_tr_b16 v[92:93], v184 offset:0x2aa0
	ds_read_b64_tr_b16 v[102:103], v184 offset:0x2ca0
	ds_read_b64_tr_b16 v[104:105], v184 offset:0x2ea0
	ds_read_b64_tr_b16 v[106:107], v184 offset:0x30c0
	ds_read_b64_tr_b16 v[108:109], v184 offset:0x32c0
	ds_read_b64_tr_b16 v[110:111], v184 offset:0x34c0
	ds_read_b64_tr_b16 v[112:113], v184 offset:0x36c0
	s_waitcnt lgkmcnt(4)
	s_nop 5
	v_mfma_f32_16x16x32_bf16 v[50:53], v[18:21], v[82:85], v[50:53]
	v_mfma_f32_16x16x32_bf16 v[18:21], v[18:21], v[86:89], v[54:57]
	v_mfma_f32_16x16x32_bf16 v[70:73], v[90:93], v[82:85], v[70:73]
	v_mfma_f32_16x16x32_bf16 v[78:81], v[90:93], v[86:89], v[78:81]
	v_mfma_f32_16x16x32_bf16 v[54:57], v[22:25], v[94:97], v[50:53]
	v_mfma_f32_16x16x32_bf16 v[22:25], v[22:25], v[98:101], v[18:21]
	v_mfma_f32_16x16x32_bf16 v[50:53], v[102:105], v[94:97], v[70:73]
	v_mfma_f32_16x16x32_bf16 v[18:21], v[102:105], v[98:101], v[78:81]
	ds_read_b64_tr_b16 v[70:71], v184 offset:0x38e0
	ds_read_b64_tr_b16 v[72:73], v184 offset:0x3ae0
	ds_read_b64_tr_b16 v[78:79], v184 offset:0x3ce0
	ds_read_b64_tr_b16 v[80:81], v184 offset:0x3ee0
	s_waitcnt lgkmcnt(4)
	v_mfma_f32_16x16x32_bf16 v[26:29], v[106:109], v[82:85], v[26:29]
	s_waitcnt lgkmcnt(0)
	v_mfma_f32_16x16x32_bf16 v[90:93], v[106:109], v[86:89], v[58:61]
	v_mfma_f32_16x16x32_bf16 v[58:61], v[110:113], v[94:97], v[26:29]
	v_mfma_f32_16x16x32_bf16 v[26:29], v[110:113], v[98:101], v[90:93]
	v_mfma_f32_16x16x32_bf16 v[30:33], v[70:73], v[82:85], v[30:33]
	v_mfma_f32_16x16x32_bf16 v[70:73], v[70:73], v[86:89], v[62:65]
	v_mfma_f32_16x16x32_bf16 v[62:65], v[78:81], v[94:97], v[30:33]
	v_mfma_f32_16x16x32_bf16 v[30:33], v[78:81], v[98:101], v[70:73]
	v_add_f32_e64 v66, v66, v68
	v_add_f32_e64 v67, v67, v69
	v_pk_add_f32 v[68:69], v[114:115], v[114:115] op_sel:[0,1] op_sel_hi:[1,0]
	v_pk_add_f32 v[66:67], v[66:67], v[66:67] op_sel:[0,1] op_sel_hi:[1,0]
	v_add_f32_e32 v74, v116, v117
	v_add_f32_e32 v76, v118, v119
	v_mov_b32_e32 v69, v120
	v_mov_b32_e32 v67, v121
	v_pk_add_f32 v[66:67], v[68:69], v[66:67]
	v_pk_add_f32 v[68:69], v[74:75], v[76:77]
	s_nop 0
	v_pk_add_f32 v[66:67], v[66:67], v[68:69]
	s_nop 0
	v_add_f32_e32 v66, v66, v67
	s_setprio 0
	ds_bpermute_b32 v67, v177, v66
	ds_bpermute_b32 v68, v177, v122
	v_mov_b32_e32 v70, v185
	s_waitcnt lgkmcnt(1)
	v_add_f32_e32 v66, v66, v67
	s_waitcnt lgkmcnt(0)
	v_add_f32_e32 v67, v122, v68
	ds_bpermute_b32 v68, v188, v66
	ds_bpermute_b32 v69, v188, v67
	s_waitcnt lgkmcnt(1)
	v_add_f32_e32 v66, v66, v68
	s_waitcnt lgkmcnt(0)
	v_add_f32_e32 v67, v67, v69
	v_rcp_f32_e32 v68, v66
	v_rcp_f32_e32 v66, v67
	v_mov_b32_e32 v67, v176
	v_mov_b32_e32 v69, v180
	s_branch .LBB0_641

; __device__ __forceinline__ unsigned xb_ld(unsigned* p)              { return __hip_atomic_load(p, __ATOMIC_RELAXED, __HIP_MEMORY_SCOPE_AGENT); }
; __device__ __forceinline__ void xcd_barrier_complete(unsigned* bar, unsigned x, unsigned& nloc, unsigned& nx) {
;     const unsigned G = gridDim.x * gridDim.y * gridDim.z;
;     unsigned sum, cnt, mine, sp = 0u;
;     for (;;) {
;         sum = 0u; cnt = 0u; mine = 0u;
; #pragma unroll
;         for (unsigned j = 0; j < 16; ++j) { const unsigned c = xb_ld(&bar[XB_XCNT(j)]); sum += c; cnt += (c > 0u) ? 1u : 0u; mine = (j == x) ? c : mine; }
;         if (sum == G) break;
;         __builtin_amdgcn_s_sleep(1);
;         if ((++sp & 255u) == 0u) { if (xb_ld(&bar[XB_TMO])) break; if (sp > XB_SPIN_CAP) { atomicAdd(&bar[XB_TMO], 1u); break; } }
;     }
;     nloc = mine > 0u ? mine : 1u; nx = cnt > 0u ? cnt : 1u;
; __device__ __forceinline__ void xcd_barrier(const XcdBarrier& b) {
;     asm volatile("s_waitcnt vmcnt(0)" ::: "memory");
;     __syncthreads();
;     if (threadIdx.x == 0) {
;         unsigned* bar = b.bar;
;         __builtin_amdgcn_s_waitcnt(0);
;         unsigned nloc = b.st[0], nx = b.st[1];
;         if (nloc == 0u) { xcd_barrier_complete(bar, b.x, nloc, nx); b.st[0] = nloc; b.st[1] = nx; }
.LBB0_653:
	s_nop 0
	s_nop 0
	s_nop 0
	s_nop 0
	s_nop 0
	s_nop 0
	s_nop 0
	s_nop 0
	s_nop 0
	s_nop 0
	s_nop 0
	s_nop 0
	s_nop 0
	s_cmp_gt_i32 s81, 8
	s_cselect_b64 s[4:5], -1, 0
	s_and_b64 s[0:1], s[10:11], s[4:5]
	s_andn2_b64 vcc, exec, s[0:1]
	s_cbranch_vccnz .LBB0_707
	s_mov_b64 s[8:9], s[96:97]
	s_getreg_b32 s0, hwreg(HW_REG_XCC_ID, 0, 4)
	s_waitcnt vmcnt(0)
	s_waitcnt vmcnt(0)
	s_barrier
	s_mov_b64 s[6:7], exec
	v_readlane_b32 s2, v255, 0
	v_readlane_b32 s3, v255, 1
	s_and_b64 s[2:3], s[6:7], s[2:3]
	s_mov_b64 exec, s[2:3]
	s_cbranch_execz .LBB0_706
	s_add_i32 s1, 0, 0x22160
	v_mov_b32_e32 v2, s1
	s_load_dwordx2 s[8:9], s[8:9], 0xe8
	s_waitcnt vmcnt(0) expcnt(0) lgkmcnt(0)
	ds_read_b32 v4, v2
	s_add_i32 s1, 0, 0x22164
	v_mov_b32_e32 v2, s1
	ds_read_b32 v2, v2
	s_and_b32 s0, s0, 15
	s_waitcnt lgkmcnt(1)
	v_cmp_ne_u32_e32 vcc, 0, v4
	s_cbranch_vccnz .LBB0_670
	s_add_u32 s10, s8, 0x4200
	s_addc_u32 s11, s9, 0
	s_add_u32 s12, s8, 0x4400
	s_addc_u32 s13, s9, 0
	s_add_u32 s14, s8, 0x4500
	s_addc_u32 s15, s9, 0
	s_add_u32 s16, s8, 0x4600
	s_addc_u32 s17, s9, 0
	s_add_u32 s18, s8, 0x4700
	s_addc_u32 s19, s9, 0
	s_add_u32 s20, s8, 0x4800
	s_addc_u32 s21, s9, 0
	s_add_u32 s22, s8, 0x4900
	s_addc_u32 s23, s9, 0
	s_add_u32 s24, s8, 0x4a00
	s_addc_u32 s25, s9, 0
	s_add_u32 s26, s8, 0x4b00
	s_addc_u32 s27, s9, 0
	s_add_u32 s28, s8, 0x4c00
	s_addc_u32 s29, s9, 0
	s_add_u32 s30, s8, 0x4d00
	s_addc_u32 s31, s9, 0
	s_add_u32 s34, s8, 0x4e00
	s_addc_u32 s35, s9, 0
	s_add_u32 s36, s8, 0x4f00
	s_addc_u32 s37, s9, 0
	s_add_u32 s38, s8, 0x5000
	s_addc_u32 s39, s9, 0
	s_load_dwordx2 s[2:3], s[96:97], 0xf8
	s_load_dword s1, s[96:97], 0x100
	s_add_u32 s40, s8, 0x5100
	s_addc_u32 s41, s9, 0
	s_add_u32 s42, s8, 0x5200
	s_addc_u32 s43, s9, 0
	s_waitcnt lgkmcnt(0)
	s_mul_i32 s2, s3, s2
	s_add_u32 s44, s8, 0x5300
	s_mul_i32 s1, s2, s1
	s_addc_u32 s45, s9, 0
	s_mov_b32 s2, 1
	v_mov_b32_e32 v18, 0
	s_branch .LBB0_658
